# v47 + combine/final-norm phase: all 32 loads of a row issued together (last 10 into spare registers, copied at first use)
# baseline (speedup 1.0000x reference)
; #define GAS __attribute__((address_space(1)))
; __device__ __forceinline__ void final_phase(Frame& F) {
;     ...
;         if (!tail) {
; #pragma unroll
;             for (int j = 0; j < 8; ++j) { const int col = 4 * (F.lane + 64 * j);
;                 const v2u ya = *(const GAS v2u*)(Y2 + s0 + col), yb = *(const GAS v2u*)(Y2 + s1 + col); const f32x4 gg = *(const GAS f32x4*)(g2 + col);
;                 f32x4 mo; mo.x = w0 * bflo(ya.x) + w1 * bflo(yb.x); mo.y = w0 * bfhi(ya.x) + w1 * bfhi(yb.x); mo.z = w0 * bflo(ya.y) + w1 * bflo(yb.y); mo.w = w0 * bfhi(ya.y) + w1 * bfhi(yb.y);
;                 { const v2u hw = hr[64 * j]; f32x4 hv; hv.x = bflo(hw.x); hv.y = bfhi(hw.x); hv.z = bflo(hw.y); hv.w = bfhi(hw.y); v[j] = hv + gg * mo; } s += (v[j].x * v[j].x + v[j].y * v[j].y) + (v[j].z * v[j].z + v[j].w * v[j].w); }
.LBB0_2191:
	s_ashr_i32 s17, s16, 31
	s_lshl_b64 s[2:3], s[16:17], 2
	s_add_i32 s0, s16, 1
	s_ashr_i32 s1, s0, 31
	v_lshlrev_b32_e32 v78, 2, v30
	v_lshlrev_b32_e32 v88, 2, v34
	v_lshlrev_b32_e32 v67, 2, v36
	v_lshlrev_b32_e32 v27, 2, v38
	v_lshlrev_b32_e32 v26, 2, v40
	v_lshlrev_b32_e32 v25, 2, v44
	v_lshlrev_b32_e32 v24, 2, v48
	v_lshlrev_b32_e32 v65, 2, v52
	s_waitcnt vmcnt(8)
	v_readfirstlane_b32 s4, v232
	v_readfirstlane_b32 s5, v233
	s_cmp_eq_u32 s4, 1
	s_cselect_b32 s17, s30, 0
	s_cmp_eq_u32 s5, 1
	s_cselect_b32 s18, s30, 0
	s_cmp_eq_u32 s4, 2
	s_cselect_b32 s17, s31, s17
	s_cmp_eq_u32 s5, 2
	s_cselect_b32 s18, s31, s18
	s_cmp_eq_u32 s4, 3
	s_cselect_b32 s17, s33, s17
	s_cmp_eq_u32 s5, 3
	s_cselect_b32 s18, s33, s18
	s_cmp_eq_u32 s4, 4
	s_cselect_b32 s17, s34, s17
	s_cmp_eq_u32 s5, 4
	s_cselect_b32 s18, s34, s18
	s_cmp_eq_u32 s4, 5
	s_cselect_b32 s17, s35, s17
	s_cmp_eq_u32 s5, 5
	s_cselect_b32 s18, s35, s18
	s_cmp_eq_u32 s4, 6
	s_cselect_b32 s17, s36, s17
	s_cmp_eq_u32 s5, 6
	s_cselect_b32 s18, s36, s18
	s_cmp_eq_u32 s4, 7
	s_cselect_b32 s17, s37, s17
	s_cmp_eq_u32 s5, 7
	s_cselect_b32 s20, s37, s18
	s_lshl_b64 s[18:19], s[0:1], 2
	v_readfirstlane_b32 s0, v234
	s_add_i32 s0, s17, s0
	s_ashr_i32 s1, s0, 31
	s_lshl_b64 s[4:5], s[0:1], 11
	v_readfirstlane_b32 s0, v235
	s_add_i32 s0, s20, s0
	s_ashr_i32 s1, s0, 31
	s_lshl_b64 s[0:1], s[0:1], 11
	s_add_u32 s2, s40, s2
	s_addc_u32 s3, s41, s3
	s_add_u32 s18, s40, s18
	s_addc_u32 s19, s41, s19
	global_load_dword v64, v29, s[2:3]
	global_load_dword v66, v29, s[18:19]
	s_ashr_i32 s2, s6, 13
	s_mul_hi_i32 s3, s2, 0xc000
	s_mul_i32 s2, s2, 0xc000
	s_add_u32 s2, s88, s2
	s_addc_u32 s3, s89, s3
	s_add_u32 s18, s2, 0x12e000
	s_addc_u32 s19, s3, 0
	s_or_b64 s[2:3], s[0:1], s[4:5]
	v_cmp_gt_u64_e32 vcc, s[2:3], v[62:63]
	s_nop 1
	v_cndmask_b32_e64 v0, 0, 1, vcc
	s_nop 0
	v_readfirstlane_b32 s2, v0
	s_bitcmp1_b32 s2, 0
	s_cselect_b64 s[20:21], -1, 0
	s_mov_b64 s[2:3], -1
	s_and_b64 vcc, exec, s[20:21]
	s_cbranch_vccnz .LBB0_2193
	global_load_dwordx2 v[18:19], v[58:59], off
	global_load_dwordx2 v[68:69], v[58:59], off offset:512
	global_load_dwordx2 v[70:71], v[58:59], off offset:1024
	v_lshl_add_u64 v[6:7], s[4:5], 1, v[56:57]
	global_load_dwordx2 v[72:73], v[6:7], off
	v_lshl_add_u64 v[4:5], s[0:1], 1, v[56:57]
	global_load_dwordx2 v[74:75], v[4:5], off
	global_load_dwordx2 v[76:77], v[6:7], off offset:512
	global_load_dwordx2 v[90:91], v[4:5], off offset:512
	global_load_dwordx2 v[92:93], v[6:7], off offset:1024
	global_load_dwordx2 v[94:95], v[4:5], off offset:1024
	global_load_dwordx4 v[8:11], v78, s[18:19]
	global_load_dwordx4 v[12:15], v88, s[18:19]
	global_load_dwordx4 v[80:83], v67, s[18:19]
	global_load_dwordx2 v[96:97], v[6:7], off offset:1536
	global_load_dwordx2 v[98:99], v[4:5], off offset:1536
	global_load_dwordx4 v[84:87], v27, s[18:19]
	global_load_dwordx2 v[100:101], v[58:59], off offset:1536
	global_load_dwordx4 v[0:3], v26, s[18:19]
	global_load_dwordx2 v[16:17], v[58:59], off offset:2048
	global_load_dwordx2 v[102:103], v[6:7], off offset:2048
	global_load_dwordx2 v[20:21], v[6:7], off offset:2560
	global_load_dwordx2 v[104:105], v[4:5], off offset:2048
	global_load_dwordx2 v[22:23], v[4:5], off offset:2560
	global_load_dwordx2 v[160:161], v[58:59], off offset:2560
	global_load_dwordx4 v[164:167], v25, s[18:19]
	global_load_dwordx2 v[162:163], v[4:5], off offset:3072
	global_load_dwordx2 v[168:169], v[6:7], off offset:3072
	global_load_dwordx2 v[170:171], v[58:59], off offset:3072
	global_load_dwordx4 v[172:175], v24, s[18:19]
	global_load_dwordx2 v[176:177], v[58:59], off offset:3584
	global_load_dwordx2 v[182:183], v[6:7], off offset:3584
	global_load_dwordx2 v[184:185], v[4:5], off offset:3584
	global_load_dwordx4 v[188:191], v65, s[18:19]
	s_mov_b64 s[2:3], 0
	s_waitcnt vmcnt(26)
	v_lshlrev_b32_e32 v116, 16, v76
	s_waitcnt vmcnt(25)
	v_lshlrev_b32_e32 v118, 16, v90
	v_and_b32_e32 v119, 0xffff0000, v90
	v_lshlrev_b32_e32 v90, 16, v91
	v_and_b32_e32 v91, 0xffff0000, v91
	v_and_b32_e32 v117, 0xffff0000, v76
	v_lshlrev_b32_e32 v76, 16, v77
	v_and_b32_e32 v77, 0xffff0000, v77
	s_waitcnt vmcnt(23)
	v_lshlrev_b32_e32 v122, 16, v94
	v_and_b32_e32 v123, 0xffff0000, v94
	v_lshlrev_b32_e32 v106, 16, v18
	v_lshlrev_b32_e32 v108, 16, v68
	v_lshlrev_b32_e32 v112, 16, v70
	v_and_b32_e32 v113, 0xffff0000, v70
	v_lshlrev_b32_e32 v114, 16, v71
	v_and_b32_e32 v115, 0xffff0000, v71
	v_lshlrev_b32_e32 v70, 16, v74
	v_and_b32_e32 v71, 0xffff0000, v74
	v_lshlrev_b32_e32 v74, 16, v75
	v_and_b32_e32 v75, 0xffff0000, v75
	v_and_b32_e32 v109, 0xffff0000, v68
	v_lshlrev_b32_e32 v110, 16, v69
	v_and_b32_e32 v111, 0xffff0000, v69
	v_lshlrev_b32_e32 v68, 16, v72
	v_and_b32_e32 v69, 0xffff0000, v72
	v_lshlrev_b32_e32 v72, 16, v73
	v_and_b32_e32 v73, 0xffff0000, v73
	v_pk_mul_f32 v[70:71], v[66:67], v[70:71] op_sel_hi:[0,1]
	v_pk_mul_f32 v[74:75], v[66:67], v[74:75] op_sel_hi:[0,1]
	v_and_b32_e32 v107, 0xffff0000, v18
	v_lshlrev_b32_e32 v18, 16, v19
	v_and_b32_e32 v19, 0xffff0000, v19
	v_pk_mul_f32 v[118:119], v[66:67], v[118:119] op_sel_hi:[0,1]
	v_pk_mul_f32 v[90:91], v[66:67], v[90:91] op_sel_hi:[0,1]
	v_pk_fma_f32 v[68:69], v[64:65], v[68:69], v[70:71] op_sel_hi:[0,1,1]
	v_pk_fma_f32 v[72:73], v[64:65], v[72:73], v[74:75] op_sel_hi:[0,1,1]
	v_lshlrev_b32_e32 v120, 16, v92
	v_and_b32_e32 v121, 0xffff0000, v92
	v_lshlrev_b32_e32 v94, 16, v95
	v_and_b32_e32 v95, 0xffff0000, v95
	v_pk_mul_f32 v[122:123], v[66:67], v[122:123] op_sel_hi:[0,1]
	v_pk_fma_f32 v[74:75], v[64:65], v[116:117], v[118:119] op_sel_hi:[0,1,1]
	v_pk_fma_f32 v[76:77], v[64:65], v[76:77], v[90:91] op_sel_hi:[0,1,1]
	s_waitcnt vmcnt(22)
; #define GAS __attribute__((address_space(1)))
; __device__ __forceinline__ void final_phase(Frame& F) {
;     ...
;             for (int j = 0; j < 8; ++j) { const int col = 4 * (F.lane + 64 * j);
;                 const v2u ya = *(const GAS v2u*)(Y2 + s0 + col), yb = *(const GAS v2u*)(Y2 + s1 + col); const f32x4 gg = *(const GAS f32x4*)(g2 + col);
;                 f32x4 mo; mo.x = w0 * bflo(ya.x) + w1 * bflo(yb.x); mo.y = w0 * bfhi(ya.x) + w1 * bfhi(yb.x); mo.z = w0 * bflo(ya.y) + w1 * bflo(yb.y); mo.w = w0 * bfhi(ya.y) + w1 * bfhi(yb.y);
;                 { const v2u hw = hr[64 * j]; f32x4 hv; hv.x = bflo(hw.x); hv.y = bfhi(hw.x); hv.z = bflo(hw.y); hv.w = bfhi(hw.y); v[j] = hv + gg * mo; } s += (v[j].x * v[j].x + v[j].y * v[j].y) + (v[j].z * v[j].z + v[j].w * v[j].w); }
	v_pk_fma_f32 v[70:71], v[8:9], v[68:69], v[106:107]
	v_pk_fma_f32 v[68:69], v[10:11], v[72:73], v[18:19]
	v_lshlrev_b32_e32 v92, 16, v93
	v_and_b32_e32 v93, 0xffff0000, v93
	v_pk_mul_f32 v[94:95], v[66:67], v[94:95] op_sel_hi:[0,1]
	v_pk_fma_f32 v[90:91], v[64:65], v[120:121], v[122:123] op_sel_hi:[0,1,1]
	s_waitcnt vmcnt(21)
	v_pk_fma_f32 v[74:75], v[12:13], v[74:75], v[108:109]
	v_pk_fma_f32 v[72:73], v[14:15], v[76:77], v[110:111]
	v_pk_mul_f32 v[12:13], v[68:69], v[68:69]
	v_pk_mul_f32 v[14:15], v[70:71], v[70:71]
	v_pk_fma_f32 v[92:93], v[64:65], v[92:93], v[94:95] op_sel_hi:[0,1,1]
	s_waitcnt vmcnt(20)
	v_pk_fma_f32 v[8:9], v[80:81], v[90:91], v[112:113]
	v_pk_mul_f32 v[18:19], v[72:73], v[72:73]
	v_pk_mul_f32 v[76:77], v[74:75], v[74:75]
	v_pk_mov_b32 v[80:81], v[14:15], v[12:13] op_sel:[1,0]
	v_mov_b32_e32 v15, v13
	v_pk_fma_f32 v[10:11], v[82:83], v[92:93], v[114:115]
	v_pk_mov_b32 v[12:13], v[76:77], v[18:19] op_sel:[1,0]
	v_mov_b32_e32 v77, v19
	v_pk_add_f32 v[18:19], v[80:81], v[14:15]
	s_waitcnt vmcnt(18)
	v_lshlrev_b32_e32 v14, 16, v98
	v_and_b32_e32 v15, 0xffff0000, v98
	v_pk_add_f32 v[76:77], v[12:13], v[76:77]
	v_lshlrev_b32_e32 v12, 16, v96
	v_and_b32_e32 v13, 0xffff0000, v96
	v_pk_mul_f32 v[14:15], v[66:67], v[14:15] op_sel_hi:[0,1]
	v_lshlrev_b32_e32 v90, 16, v99
	v_and_b32_e32 v91, 0xffff0000, v99
	v_pk_fma_f32 v[12:13], v[64:65], v[12:13], v[14:15] op_sel_hi:[0,1,1]
	v_lshlrev_b32_e32 v14, 16, v97
	v_and_b32_e32 v15, 0xffff0000, v97
	v_pk_mul_f32 v[90:91], v[66:67], v[90:91] op_sel_hi:[0,1]
	v_pk_fma_f32 v[14:15], v[64:65], v[14:15], v[90:91] op_sel_hi:[0,1,1]
	s_waitcnt vmcnt(16)
	v_lshlrev_b32_e32 v90, 16, v101
	v_and_b32_e32 v91, 0xffff0000, v101
	v_lshlrev_b32_e32 v96, 16, v100
	v_and_b32_e32 v97, 0xffff0000, v100
	v_pk_fma_f32 v[14:15], v[86:87], v[14:15], v[90:91]
	v_pk_fma_f32 v[12:13], v[84:85], v[12:13], v[96:97]
	v_pk_add_f32 v[18:19], v[18:19], v[18:19] op_sel:[0,1] op_sel_hi:[1,0]
	v_mul_f32_e32 v28, v12, v12
	v_mul_f32_e32 v79, v13, v13
	v_pk_add_f32 v[76:77], v[76:77], v[76:77] op_sel:[0,1] op_sel_hi:[1,0]
	v_mov_b32_e32 v19, v28
	v_mov_b32_e32 v77, v79
	v_mul_f32_e32 v28, v9, v9
	v_mul_f32_e32 v84, v14, v14
	v_pk_add_f32 v[18:19], v[18:19], v[76:77]
	v_pk_fma_f32 v[76:77], v[8:9], v[8:9], v[28:29] op_sel_hi:[1,1,0]
	v_mul_f32_e32 v28, v11, v11
	v_mul_f32_e32 v86, v15, v15
	v_mov_b32_e32 v77, v84
	v_pk_fma_f32 v[84:85], v[10:11], v[10:11], v[28:29] op_sel_hi:[1,1,0]
	v_mov_b32_e32 v85, v86
	v_pk_add_f32 v[76:77], v[76:77], v[84:85]
	s_waitcnt vmcnt(11)
	v_lshlrev_b32_e32 v4, 16, v104
	v_and_b32_e32 v5, 0xffff0000, v104
	v_lshlrev_b32_e32 v6, 16, v102
	v_and_b32_e32 v7, 0xffff0000, v102
	v_pk_mul_f32 v[4:5], v[66:67], v[4:5] op_sel_hi:[0,1]
	v_pk_add_f32 v[76:77], v[18:19], v[76:77]
	v_pk_fma_f32 v[18:19], v[64:65], v[6:7], v[4:5] op_sel_hi:[0,1,1]
	v_lshlrev_b32_e32 v6, 16, v105
	v_and_b32_e32 v7, 0xffff0000, v105
	v_lshlrev_b32_e32 v4, 16, v103
	v_and_b32_e32 v5, 0xffff0000, v103
	v_pk_mul_f32 v[6:7], v[66:67], v[6:7] op_sel_hi:[0,1]
	v_pk_fma_f32 v[100:101], v[64:65], v[4:5], v[6:7] op_sel_hi:[0,1,1]
	v_lshlrev_b32_e32 v102, 16, v16
	v_and_b32_e32 v103, 0xffff0000, v16
	v_lshlrev_b32_e32 v104, 16, v17
	v_and_b32_e32 v105, 0xffff0000, v17
	v_pk_fma_f32 v[16:17], v[0:1], v[18:19], v[102:103]
	v_pk_fma_f32 v[18:19], v[2:3], v[100:101], v[104:105]
	v_pk_mul_f32 v[2:3], v[16:17], v[16:17]
	v_pk_mul_f32 v[0:1], v[18:19], v[18:19]
	v_pk_add_f32 v[76:77], v[76:77], v[76:77] op_sel:[0,1] op_sel_hi:[1,0]
	v_pk_mov_b32 v[100:101], v[2:3], v[0:1] op_sel:[1,0]
	v_mov_b32_e32 v3, v1
	v_pk_add_f32 v[100:101], v[100:101], v[2:3]
	s_waitcnt vmcnt(10)
; #define GAS __attribute__((address_space(1)))
; __device__ __forceinline__ void final_phase(Frame& F) {
;     ...
;             for (int j = 0; j < 8; ++j) { const int col = 4 * (F.lane + 64 * j);
;                 const v2u ya = *(const GAS v2u*)(Y2 + s0 + col), yb = *(const GAS v2u*)(Y2 + s1 + col); const f32x4 gg = *(const GAS f32x4*)(g2 + col);
;                 f32x4 mo; mo.x = w0 * bflo(ya.x) + w1 * bflo(yb.x); mo.y = w0 * bfhi(ya.x) + w1 * bfhi(yb.x); mo.z = w0 * bflo(ya.y) + w1 * bflo(yb.y); mo.w = w0 * bfhi(ya.y) + w1 * bfhi(yb.y);
;                 { const v2u hw = hr[64 * j]; f32x4 hv; hv.x = bflo(hw.x); hv.y = bfhi(hw.x); hv.z = bflo(hw.y); hv.w = bfhi(hw.y); v[j] = hv + gg * mo; } s += (v[j].x * v[j].x + v[j].y * v[j].y) + (v[j].z * v[j].z + v[j].w * v[j].w); }
	v_lshlrev_b32_e32 v2, 16, v22
	v_and_b32_e32 v3, 0xffff0000, v22
	v_lshlrev_b32_e32 v0, 16, v20
	v_and_b32_e32 v1, 0xffff0000, v20
	v_pk_mul_f32 v[2:3], v[66:67], v[2:3] op_sel_hi:[0,1]
	v_pk_fma_f32 v[0:1], v[64:65], v[0:1], v[2:3] op_sel_hi:[0,1,1]
	v_lshlrev_b32_e32 v2, 16, v21
	v_and_b32_e32 v3, 0xffff0000, v21
	v_lshlrev_b32_e32 v20, 16, v23
	v_and_b32_e32 v21, 0xffff0000, v23
	v_pk_mul_f32 v[20:21], v[66:67], v[20:21] op_sel_hi:[0,1]
	v_pk_fma_f32 v[2:3], v[64:65], v[2:3], v[20:21] op_sel_hi:[0,1,1]
	s_waitcnt vmcnt(9)
	v_mov_b32_e32 v94, v160
	v_mov_b32_e32 v95, v161
	v_lshlrev_b32_e32 v22, 16, v95
	v_and_b32_e32 v23, 0xffff0000, v95
	v_lshlrev_b32_e32 v20, 16, v94
	v_and_b32_e32 v21, 0xffff0000, v94
	s_waitcnt vmcnt(8)
	v_mov_b32_e32 v80, v164
	v_mov_b32_e32 v81, v165
	v_mov_b32_e32 v82, v166
	v_mov_b32_e32 v83, v167
	v_pk_fma_f32 v[22:23], v[82:83], v[2:3], v[22:23]
	s_waitcnt vmcnt(7)
	v_mov_b32_e32 v108, v162
	v_mov_b32_e32 v109, v163
	v_lshlrev_b32_e32 v2, 16, v108
	v_and_b32_e32 v3, 0xffff0000, v108
	v_pk_fma_f32 v[20:21], v[80:81], v[0:1], v[20:21]
	s_waitcnt vmcnt(6)
	v_mov_b32_e32 v106, v168
	v_mov_b32_e32 v107, v169
	v_lshlrev_b32_e32 v0, 16, v106
	v_and_b32_e32 v1, 0xffff0000, v106
	v_pk_mul_f32 v[2:3], v[66:67], v[2:3] op_sel_hi:[0,1]
	v_lshlrev_b32_e32 v80, 16, v109
	v_and_b32_e32 v81, 0xffff0000, v109
	v_pk_fma_f32 v[0:1], v[64:65], v[0:1], v[2:3] op_sel_hi:[0,1,1]
	v_lshlrev_b32_e32 v2, 16, v107
	v_and_b32_e32 v3, 0xffff0000, v107
	v_pk_mul_f32 v[80:81], v[66:67], v[80:81] op_sel_hi:[0,1]
	v_pk_fma_f32 v[2:3], v[64:65], v[2:3], v[80:81] op_sel_hi:[0,1,1]
	s_waitcnt vmcnt(5)
	v_mov_b32_e32 v98, v170
	v_mov_b32_e32 v99, v171
	v_lshlrev_b32_e32 v80, 16, v98
	v_and_b32_e32 v81, 0xffff0000, v98
	v_lshlrev_b32_e32 v82, 16, v99
	s_waitcnt vmcnt(4)
	v_mov_b32_e32 v90, v172
	v_mov_b32_e32 v91, v173
	v_mov_b32_e32 v92, v174
	v_mov_b32_e32 v93, v175
	v_pk_fma_f32 v[0:1], v[90:91], v[0:1], v[80:81]
	v_and_b32_e32 v83, 0xffff0000, v99
	v_mul_f32_e32 v28, v0, v0
	v_mul_f32_e32 v79, v1, v1
	v_pk_add_f32 v[80:81], v[100:101], v[100:101] op_sel:[0,1] op_sel_hi:[1,0]
	v_pk_fma_f32 v[2:3], v[92:93], v[2:3], v[82:83]
	v_mov_b32_e32 v77, v28
	v_mov_b32_e32 v81, v79
	v_mul_f32_e32 v28, v21, v21
	v_mul_f32_e32 v82, v2, v2
	v_pk_add_f32 v[76:77], v[76:77], v[80:81]
	v_pk_fma_f32 v[80:81], v[20:21], v[20:21], v[28:29] op_sel_hi:[1,1,0]
	v_mul_f32_e32 v28, v23, v23
	v_mul_f32_e32 v89, v3, v3
	v_mov_b32_e32 v81, v82
	v_pk_fma_f32 v[82:83], v[22:23], v[22:23], v[28:29] op_sel_hi:[1,1,0]
	s_nop 0
	v_mov_b32_e32 v83, v89
	v_pk_add_f32 v[80:81], v[80:81], v[82:83]
	s_waitcnt vmcnt(1)
	v_mov_b32_e32 v96, v176
	v_mov_b32_e32 v97, v177
	v_mov_b32_e32 v84, v182
	v_mov_b32_e32 v85, v183
	v_mov_b32_e32 v86, v184
	v_mov_b32_e32 v87, v185
	v_lshlrev_b32_e32 v82, 16, v87
	v_pk_add_f32 v[76:77], v[76:77], v[80:81]
	v_lshlrev_b32_e32 v80, 16, v86
	v_and_b32_e32 v81, 0xffff0000, v86
	v_add_f32_e32 v28, v76, v77
	v_lshlrev_b32_e32 v76, 16, v84
	v_and_b32_e32 v77, 0xffff0000, v84
	v_pk_mul_f32 v[80:81], v[66:67], v[80:81] op_sel_hi:[0,1]
	v_and_b32_e32 v83, 0xffff0000, v87
	v_pk_fma_f32 v[76:77], v[64:65], v[76:77], v[80:81] op_sel_hi:[0,1,1]
	v_lshlrev_b32_e32 v80, 16, v85
	v_and_b32_e32 v81, 0xffff0000, v85
	v_pk_mul_f32 v[82:83], v[66:67], v[82:83] op_sel_hi:[0,1]
	v_pk_fma_f32 v[80:81], v[64:65], v[80:81], v[82:83] op_sel_hi:[0,1,1]
	v_lshlrev_b32_e32 v82, 16, v96
	v_and_b32_e32 v83, 0xffff0000, v96
	v_lshlrev_b32_e32 v84, 16, v97
	v_and_b32_e32 v85, 0xffff0000, v97
	s_waitcnt vmcnt(0)
	v_mov_b32_e32 v4, v188
	v_mov_b32_e32 v5, v189
	v_mov_b32_e32 v6, v190
	v_mov_b32_e32 v7, v191
	v_pk_fma_f32 v[6:7], v[6:7], v[80:81], v[84:85]
	v_pk_fma_f32 v[4:5], v[4:5], v[76:77], v[82:83]
